# speedup vs baseline: 1.0394x; 1.0133x over previous
.LBB1_2:
	s_load_dwordx2 s[4:5], s[0:1], 0x20
	s_load_dwordx8 s[12:19], s[0:1], 0x0
	s_load_dwordx2 s[20:21], s[0:1], 0x28
	s_lshr_b32 s3, s2, 5
	s_cmpk_gt_u32 s2, 0x2ff
	s_cbranch_scc0 .LBB1_4
	s_sub_i32 s6, s3, 24
	s_sub_i32 s7, 35, s3
	s_cmpk_lt_u32 s2, 0x380
	s_cselect_b32 s10, s6, s7
	s_cbranch_execz .LBB1_5
	s_branch .LBB1_6

.LBB1_6:
	v_and_b32_e32 v1, 31, v0
	v_lshl_or_b32 v2, s10, 5, v1
	v_ashrrev_i32_e32 v3, 31, v2
	s_waitcnt lgkmcnt(0)
	v_lshl_add_u64 v[2:3], v[2:3], 2, s[4:5]
	global_load_dword v104, v[2:3], off
	s_mov_b32 s11, 0
	v_lshrrev_b32_e32 v2, 2, v0
	v_and_b32_e32 v1, 15, v0
	s_lshl_b32 s5, s10, 6
	v_and_b32_e32 v2, 48, v2
	s_and_b32 s3, s2, 31
	v_or3_b32 v86, s5, v2, v1
	s_lshl_b32 s10, s3, 11
	v_ashrrev_i32_e32 v87, 31, v86
	v_lshl_add_u64 v[2:3], v[86:87], 0, s[10:11]
	v_lshlrev_b64 v[2:3], 7, v[2:3]
	v_lshl_add_u64 v[2:3], s[12:13], 0, v[2:3]
	v_mov_b32_e32 v5, 0
	v_and_b32_e32 v4, 48, v0
	v_lshl_add_u64 v[10:11], v[2:3], 0, v[4:5]
	global_load_dwordx4 v[2:5], v[10:11], off
	global_load_dwordx4 v[6:9], v[10:11], off offset:64
	v_bfe_u32 v10, v0, 4, 2
	v_and_b32_e32 v11, 63, v0
	v_lshlrev_b32_e32 v88, 3, v10
	s_lshl_b32 s1, s10, 7
	v_lshrrev_b32_e32 v13, 3, v0
	s_add_u32 s12, s14, s1
	v_mov_b32_e32 v12, 0
	v_lshlrev_b32_e32 v32, 7, v13
	s_addc_u32 s13, s15, 0
	v_mov_b32_e32 v33, v12
	v_lshl_add_u64 v[14:15], s[12:13], 0, v[32:33]
	s_add_u32 s12, s16, s1
	v_lshlrev_b32_e32 v90, 4, v0
	s_addc_u32 s13, s17, 0
	v_mov_b32_e32 v91, v12
	v_lshl_add_u64 v[94:95], s[12:13], 0, v[90:91]
	v_and_b32_e32 v16, 0x70, v90
	v_mov_b32_e32 v17, v12
	v_lshl_add_u64 v[92:93], v[14:15], 0, v[16:17]
	v_lshl_add_u64 v[96:97], v[86:87], 3, s[18:19]
	s_mov_b32 s0, 0
	s_lshl_b32 s12, s0, 6
	s_ashr_i32 s1, s0, 31
	s_lshl_b64 s[14:15], s[0:1], 13
	s_ashr_i32 s13, s12, 31
	v_lshl_add_u64 v[26:27], v[94:95], 0, s[14:15]
	s_lshl_b64 s[14:15], s[12:13], 7
	s_or_b32 s12, s12, 32
	s_movk_i32 s5, 0x1000
	global_load_dwordx4 v[14:17], v[26:27], off
	s_ashr_i32 s13, s12, 31
	v_add_co_u32_e32 v26, vcc, s5, v26
	v_lshl_add_u64 v[28:29], v[92:93], 0, s[14:15]
	s_lshl_b64 s[12:13], s[12:13], 7
	v_addc_co_u32_e32 v27, vcc, 0, v27, vcc
	v_lshl_add_u64 v[30:31], v[92:93], 0, s[12:13]
	global_load_dwordx4 v[22:25], v[28:29], off
	global_load_dwordx4 v[18:21], v[30:31], off
	global_load_dwordx4 v[26:29], v[26:27], off
	s_lshl_b64 s[12:13], s[0:1], 14
	v_lshl_add_u64 v[30:31], v[96:97], 0, s[12:13]
	global_load_dwordx2 v[102:103], v[30:31], off
	s_waitcnt vmcnt(7)
	v_cmp_ne_u32_e64 s[8:9], 0, v104
	v_cmp_eq_u32_e64 s[6:7], 2, v104
	s_cmp_eq_u32 s8, 0
	v_cmp_eq_u32_e64 s[4:5], 3, v104
	s_cbranch_scc1 .LBB1_48
	s_branch .LBB1_10

.LBB1_16:
	s_cmp_eq_u32 s0, 0
	s_cbranch_scc1 .Lat_spec_ok
	s_lshl_b32 s12, s0, 6
	s_ashr_i32 s1, s0, 31
	s_lshl_b64 s[14:15], s[0:1], 13
	s_ashr_i32 s13, s12, 31
	v_lshl_add_u64 v[106:107], v[94:95], 0, s[14:15]
	s_lshl_b64 s[14:15], s[12:13], 7
	s_or_b32 s12, s12, 32
	s_movk_i32 s5, 0x1000
	global_load_dwordx4 v[14:17], v[106:107], off
	s_ashr_i32 s13, s12, 31
	v_add_co_u32_e32 v106, vcc, s5, v106
	v_lshl_add_u64 v[108:109], v[92:93], 0, s[14:15]
	s_lshl_b64 s[12:13], s[12:13], 7
	v_addc_co_u32_e32 v107, vcc, 0, v107, vcc
	v_lshl_add_u64 v[110:111], v[92:93], 0, s[12:13]
	global_load_dwordx4 v[22:25], v[108:109], off
	global_load_dwordx4 v[18:21], v[110:111], off
	global_load_dwordx4 v[26:29], v[106:107], off
	s_lshl_b64 s[12:13], s[0:1], 14
	v_lshl_add_u64 v[110:111], v[96:97], 0, s[12:13]
	global_load_dwordx2 v[102:103], v[110:111], off
.Lat_spec_ok:
	v_and_b32_e32 v31, 7, v0
	v_bitop3_b32 v33, v10, v0, 7 bitop3:0x78
	v_lshlrev_b32_e32 v1, 7, v1
	v_mbcnt_lo_u32_b32 v34, -1, 0
	v_lshlrev_b32_e32 v89, 4, v33
	v_bitop3_b32 v31, v10, v31, 4 bitop3:0x36
	v_xor_b32_e32 v33, v13, v0
	v_mov_b32_e32 v13, v12
	v_lshlrev_b32_e32 v87, 4, v11
	s_movk_i32 s1, 0x70
	v_lshlrev_b32_e32 v98, 2, v10
	v_mov_b32_e32 v10, v12
	v_mov_b32_e32 v11, v12
	v_mbcnt_hi_u32_b32 v0, -1, v34
	v_lshl_or_b32 v91, v31, 4, v1
	v_lshlrev_b32_e32 v31, 4, v33
	v_mov_b64_e32 v[36:37], v[12:13]
	v_mov_b64_e32 v[40:41], v[12:13]
	v_mov_b64_e32 v[44:45], v[12:13]
	v_mov_b64_e32 v[48:49], v[12:13]
	v_mov_b64_e32 v[52:53], v[12:13]
	s_mov_b32 s17, 0
	v_mov_b64_e32 v[100:101], 0
	s_mov_b64 s[14:15], -1
	s_mov_b32 s5, 0xff800000
	s_mov_b32 s7, 0x41000000
	s_mov_b32 s12, 0x3c003c00
	v_mov_b32_e32 v30, 0x3c003c00
	v_mov_b32_e32 v54, v12
	v_mov_b64_e32 v[34:35], v[10:11]
	v_mov_b64_e32 v[38:39], v[10:11]
	v_mov_b64_e32 v[42:43], v[10:11]
	v_mov_b64_e32 v[46:47], v[10:11]
	v_mov_b64_e32 v[50:51], v[10:11]
	v_and_or_b32 v99, v31, s1, v32
	s_mov_b32 s9, 0
	s_waitcnt vmcnt(3)
	ds_write_b128 v99, v[22:25]
	ds_write_b128 v90, v[14:17] offset:8192
	s_waitcnt vmcnt(2)
	ds_write_b128 v99, v[18:21] offset:4096
	s_waitcnt vmcnt(1)
	ds_write_b128 v90, v[26:29] offset:12288
	s_waitcnt vmcnt(0)
	s_waitcnt lgkmcnt(0)
	s_barrier
	s_cmp_gt_i32 s11, 3
	s_cbranch_scc0 .LBB1_20

.LBB1_44:
	v_exp_f32_e32 v10, v68
	v_exp_f32_e32 v11, v69
	v_exp_f32_e32 v32, v64
	v_exp_f32_e32 v13, v70
	v_exp_f32_e32 v31, v71
	v_cvt_pkrtz_f16_f32 v64, v10, v11
	v_add_u32_e32 v10, s10, v87
	ds_read_b128 v[72:75], v10 offset:8192
	ds_read_b128 v[76:79], v10 offset:10240
	v_exp_f32_e32 v33, v65
	v_exp_f32_e32 v54, v66
	v_exp_f32_e32 v55, v67
	ds_read_b128 v[80:83], v10 offset:12288
	ds_read_b128 v[106:109], v10 offset:9216
	s_mov_b32 s14, s12
	s_mov_b32 s15, s12
	s_mov_b32 s13, s12
	v_mov_b64_e32 v[70:71], s[14:15]
	v_cvt_pkrtz_f16_f32 v65, v13, v31
	v_cvt_pkrtz_f16_f32 v67, v54, v55
	v_cvt_pkrtz_f16_f32 v66, v32, v33
	v_exp_f32_e32 v84, v60
	v_exp_f32_e32 v85, v61
	v_mov_b64_e32 v[68:69], s[12:13]
	v_exp_f32_e32 v11, v62
	s_waitcnt lgkmcnt(3)
	v_mfma_f32_16x16x32_f16 v[46:49], v[72:75], v[64:67], v[46:49]
	v_exp_f32_e32 v13, v63
	ds_read_b128 v[60:63], v10 offset:14336
	ds_read_b128 v[110:113], v10 offset:11264
	v_exp_f32_e32 v31, v56
	s_waitcnt lgkmcnt(4)
	v_mfma_f32_16x16x32_f16 v[42:45], v[76:79], v[64:67], v[42:45]
	v_exp_f32_e32 v72, v57
	ds_read_b128 v[54:57], v10 offset:13312
	v_exp_f32_e32 v73, v58
	s_waitcnt lgkmcnt(4)
	v_mfma_f32_16x16x32_f16 v[38:41], v[80:83], v[64:67], v[38:41]
	ds_read_b128 v[78:81], v10 offset:15360
	v_exp_f32_e32 v74, v59
	v_cvt_pkrtz_f16_f32 v58, v84, v85
	v_mfma_f32_16x16x32_f16 v[50:53], v[68:71], v[64:67], v[50:53]
	v_cvt_pkrtz_f16_f32 v59, v11, v13
	s_waitcnt lgkmcnt(3)
	v_mfma_f32_16x16x32_f16 v[34:37], v[60:63], v[64:67], v[34:37]
	v_cvt_pkrtz_f16_f32 v61, v73, v74
	v_cvt_pkrtz_f16_f32 v60, v31, v72
	s_nop 1
	v_mfma_f32_16x16x32_f16 v[50:53], v[68:71], v[58:61], v[50:53]
	v_mfma_f32_16x16x32_f16 v[46:49], v[106:109], v[58:61], v[46:49]
	s_waitcnt lgkmcnt(2)
	v_mfma_f32_16x16x32_f16 v[42:45], v[110:113], v[58:61], v[42:45]
	s_waitcnt lgkmcnt(1)
	v_mfma_f32_16x16x32_f16 v[38:41], v[54:57], v[58:61], v[38:41]
	s_waitcnt lgkmcnt(0)
	v_mfma_f32_16x16x32_f16 v[34:37], v[78:81], v[58:61], v[34:37]
	s_andn2_b64 vcc, exec, s[18:19]
	s_cbranch_vccnz .Lat_exit4
	s_xor_b32 s9, s9, 1
	s_lshl_b32 s10, s9, 14
	s_waitcnt vmcnt(0)
	v_or_b32_e32 v10, s10, v99
	v_mov_b64_e32 v[102:103], v[100:101]
	v_or_b32_e32 v11, s10, v90
	ds_write_b128 v10, v[22:25]
	ds_write_b128 v11, v[14:17] offset:8192
	ds_write_b128 v10, v[18:21] offset:4096
	ds_write_b128 v11, v[26:29] offset:12288
	s_mov_b64 s[14:15], s[0:1]
	s_mov_b32 s0, s16
	v_mov_b32_e32 v54, v104
	s_waitcnt lgkmcnt(0)
	s_barrier
	s_cmp_gt_i32 s11, 3
	s_cbranch_scc1 .LBB1_17
	s_branch .LBB1_20
.Lat_exit4:
	s_nop 7
	v_mov_b64_e32 v[58:59], v[34:35]
	v_mov_b64_e32 v[60:61], v[36:37]
	v_mov_b64_e32 v[62:63], v[38:39]
	v_mov_b64_e32 v[64:65], v[40:41]
	v_mov_b64_e32 v[66:67], v[42:43]
	v_mov_b64_e32 v[68:69], v[44:45]
	v_mov_b64_e32 v[70:71], v[46:47]
	v_mov_b64_e32 v[72:73], v[48:49]
	v_mov_b64_e32 v[74:75], v[50:51]
	v_mov_b64_e32 v[76:77], v[52:53]
	s_branch .LBB1_47

.LBB3_1:
	s_lshl_b32 s12, s3, 15
	v_or_b32_e32 v67, s12, v65
	s_waitcnt lgkmcnt(0)
	v_mfma_f32_16x16x32_f16 v[54:57], v[22:25], v[10:13], v[54:57]
	ds_read_b128 v[68:71], v67 offset:1024
	ds_read_b128 v[72:75], v67 offset:3072
	v_or_b32_e32 v67, s12, v64
	v_mfma_f32_16x16x32_f16 v[50:53], v[18:21], v[10:13], v[50:53]
	ds_read_b128 v[76:79], v67 offset:17408
	ds_read_b128 v[80:83], v67 offset:19456
	s_add_i32 s3, s3, 1
	v_mfma_f32_16x16x32_f16 v[46:49], v[26:29], v[10:13], v[46:49]
	ds_read_b128 v[84:87], v67 offset:21504
	ds_read_b128 v[88:91], v67 offset:23552
	v_mfma_f32_16x16x32_f16 v[42:45], v[14:17], v[10:13], v[42:45]
	v_mfma_f32_16x16x32_f16 v[38:41], v[22:25], v[6:9], v[38:41]
	v_mfma_f32_16x16x32_f16 v[34:37], v[18:21], v[6:9], v[34:37]
	v_mfma_f32_16x16x32_f16 v[30:33], v[26:29], v[6:9], v[30:33]
	v_mfma_f32_16x16x32_f16 v[2:5], v[14:17], v[6:9], v[2:5]
	v_or_b32_e32 v10, s12, v66
	v_lshl_add_u64 v[6:7], v[60:61], 0, s[4:5]
	v_readfirstlane_b32 s12, v10
	v_lshl_add_u64 v[8:9], v[6:7], 0, s[6:7]
	s_mov_b32 m0, s12
	s_waitcnt vmcnt(4) lgkmcnt(0)
	s_barrier
	global_load_lds_dwordx4 v[8:9], off
	v_or_b32_e32 v8, 0x2000, v10
	v_lshl_add_u64 v[6:7], v[6:7], 0, s[10:11]
	v_readfirstlane_b32 s12, v8
	s_mov_b32 m0, s12
	v_or_b32_e32 v11, 0x4000, v10
	global_load_lds_dwordx4 v[6:7], off
	v_lshl_add_u64 v[6:7], v[58:59], 0, s[4:5]
	v_readfirstlane_b32 s12, v11
	v_lshl_add_u64 v[8:9], v[6:7], 0, s[6:7]
	s_mov_b32 m0, s12
	v_lshl_add_u64 v[6:7], v[6:7], 0, s[10:11]
	global_load_lds_dwordx4 v[8:9], off
	v_or_b32_e32 v8, 0x6000, v10
	s_cmp_lg_u32 s3, 3
	v_readfirstlane_b32 s12, v8
	s_mov_b32 m0, s12
	s_cselect_b32 s3, s3, 0
	global_load_lds_dwordx4 v[6:7], off
	s_lshl_b32 s12, s3, 15
	v_or_b32_e32 v6, s12, v65
	v_or_b32_e32 v14, s12, v64
	s_waitcnt lgkmcnt(0)
	v_mfma_f32_16x16x32_f16 v[54:57], v[76:79], v[68:71], v[54:57]
	ds_read_b128 v[10:13], v6
	ds_read_b128 v[6:9], v6 offset:2048
	v_mfma_f32_16x16x32_f16 v[50:53], v[80:83], v[68:71], v[50:53]
	ds_read_b128 v[22:25], v14 offset:16384
	ds_read_b128 v[18:21], v14 offset:18432
	v_mfma_f32_16x16x32_f16 v[46:49], v[84:87], v[68:71], v[46:49]
	ds_read_b128 v[26:29], v14 offset:20480
	ds_read_b128 v[14:17], v14 offset:22528
	v_mfma_f32_16x16x32_f16 v[42:45], v[88:91], v[68:71], v[42:45]
	v_mfma_f32_16x16x32_f16 v[38:41], v[76:79], v[72:75], v[38:41]
	v_mfma_f32_16x16x32_f16 v[34:37], v[80:83], v[72:75], v[34:37]
	v_mfma_f32_16x16x32_f16 v[30:33], v[84:87], v[72:75], v[30:33]
	v_mfma_f32_16x16x32_f16 v[2:5], v[88:91], v[72:75], v[2:5]
	s_add_u32 s4, s4, 0x80
	s_addc_u32 s5, s5, 0
	s_cmpk_eq_i32 s4, 0x680
	s_cbranch_scc0 .LBB3_1
	s_waitcnt lgkmcnt(0)
	v_mfma_f32_16x16x32_f16 v[54:57], v[22:25], v[10:13], v[54:57]
	ds_read_b128 v[58:61], v65 offset:33792
	ds_read_b128 v[66:69], v65 offset:35840
	v_mfma_f32_16x16x32_f16 v[50:53], v[18:21], v[10:13], v[50:53]
	ds_read_b128 v[70:73], v64 offset:50176
	ds_read_b128 v[74:77], v64 offset:52224
	v_mfma_f32_16x16x32_f16 v[46:49], v[26:29], v[10:13], v[46:49]
	ds_read_b128 v[78:81], v64 offset:54272
	ds_read_b128 v[82:85], v64 offset:56320
	v_mfma_f32_16x16x32_f16 v[10:13], v[14:17], v[10:13], v[42:45]
	v_mfma_f32_16x16x32_f16 v[22:25], v[22:25], v[6:9], v[38:41]
	v_mfma_f32_16x16x32_f16 v[18:21], v[18:21], v[6:9], v[34:37]
	v_mfma_f32_16x16x32_f16 v[26:29], v[26:29], v[6:9], v[30:33]
	v_mfma_f32_16x16x32_f16 v[2:5], v[14:17], v[6:9], v[2:5]
	v_or_b32_e32 v14, 0x10000, v65
	s_nop 0
	v_add_u32_e32 v30, 0x10800, v65
	s_waitcnt vmcnt(4) lgkmcnt(0)
	s_barrier
	s_waitcnt lgkmcnt(0)
	v_mfma_f32_16x16x32_f16 v[6:9], v[70:73], v[58:61], v[54:57]
	ds_read_b128 v[14:17], v14
	ds_read_b128 v[30:33], v30
	v_or_b32_e32 v38, 0x14000, v64
	v_mfma_f32_16x16x32_f16 v[34:37], v[74:77], v[58:61], v[50:53]
	v_add_u32_e32 v42, 0x14800, v64
	v_add_u32_e32 v54, 0x15800, v64
	ds_read_b128 v[38:41], v38
	v_add_u32_e32 v50, 0x15000, v64
	ds_read_b128 v[42:45], v42
	v_mfma_f32_16x16x32_f16 v[46:49], v[78:81], v[58:61], v[46:49]
	ds_read_b128 v[50:53], v50
	ds_read_b128 v[54:57], v54
	v_mfma_f32_16x16x32_f16 v[10:13], v[82:85], v[58:61], v[10:13]
	v_mfma_f32_16x16x32_f16 v[22:25], v[70:73], v[66:69], v[22:25]
	v_mfma_f32_16x16x32_f16 v[18:21], v[74:77], v[66:69], v[18:21]
	v_mfma_f32_16x16x32_f16 v[26:29], v[78:81], v[66:69], v[26:29]
	v_mfma_f32_16x16x32_f16 v[2:5], v[82:85], v[66:69], v[2:5]
	v_add_u32_e32 v58, 0x10400, v65
	v_add_u32_e32 v66, 0x10c00, v65
	v_add_u32_e32 v70, 0x14400, v64
	v_add_u32_e32 v74, 0x14c00, v64
	v_add_u32_e32 v78, 0x15400, v64
	v_add_u32_e32 v82, 0x15c00, v64
	s_waitcnt lgkmcnt(0)
	v_mfma_f32_16x16x32_f16 v[6:9], v[38:41], v[14:17], v[6:9]
	ds_read_b128 v[58:61], v58
	ds_read_b128 v[66:69], v66
	v_mfma_f32_16x16x32_f16 v[34:37], v[42:45], v[14:17], v[34:37]
	ds_read_b128 v[70:73], v70
	ds_read_b128 v[74:77], v74
	v_mfma_f32_16x16x32_f16 v[46:49], v[50:53], v[14:17], v[46:49]
	ds_read_b128 v[78:81], v78
	ds_read_b128 v[82:85], v82
	v_mfma_f32_16x16x32_f16 v[10:13], v[54:57], v[14:17], v[10:13]
	v_mfma_f32_16x16x32_f16 v[14:17], v[38:41], v[30:33], v[22:25]
	v_mfma_f32_16x16x32_f16 v[18:21], v[42:45], v[30:33], v[18:21]
	v_mfma_f32_16x16x32_f16 v[22:25], v[50:53], v[30:33], v[26:29]
	v_mfma_f32_16x16x32_f16 v[2:5], v[54:57], v[30:33], v[2:5]
	s_waitcnt vmcnt(0) lgkmcnt(0)
	s_waitcnt lgkmcnt(0)
	v_mfma_f32_16x16x32_f16 v[6:9], v[70:73], v[58:61], v[6:9]
	s_barrier
	ds_read_b128 v[26:29], v65
	ds_read_b128 v[30:33], v65 offset:2048
	v_mfma_f32_16x16x32_f16 v[34:37], v[74:77], v[58:61], v[34:37]
	ds_read_b128 v[38:41], v64 offset:16384
	ds_read_b128 v[42:45], v64 offset:18432
	v_mfma_f32_16x16x32_f16 v[46:49], v[78:81], v[58:61], v[46:49]
	ds_read_b128 v[50:53], v64 offset:20480
	ds_read_b128 v[54:57], v64 offset:22528
	v_mfma_f32_16x16x32_f16 v[10:13], v[82:85], v[58:61], v[10:13]
	v_mfma_f32_16x16x32_f16 v[14:17], v[70:73], v[66:69], v[14:17]
	v_mfma_f32_16x16x32_f16 v[18:21], v[74:77], v[66:69], v[18:21]
	v_mfma_f32_16x16x32_f16 v[22:25], v[78:81], v[66:69], v[22:25]
	v_mfma_f32_16x16x32_f16 v[2:5], v[82:85], v[66:69], v[2:5]
	s_waitcnt lgkmcnt(0)
	v_mfma_f32_16x16x32_f16 v[6:9], v[38:41], v[26:29], v[6:9]
	ds_read_b128 v[58:61], v64 offset:19456
	s_lshl_b64 s[0:1], s[0:1], 2
	v_lshl_add_u32 v63, v63, 5, s2
	v_mfma_f32_16x16x32_f16 v[34:37], v[42:45], v[26:29], v[34:37]
	s_add_u32 s0, s8, s0
	v_and_or_b32 v0, v0, 15, v63
	s_addc_u32 s1, s9, s1
	v_mfma_f32_16x16x32_f16 v[46:49], v[50:53], v[26:29], v[46:49]
	v_and_b32_e32 v1, 12, v1
	v_mfma_f32_16x16x32_f16 v[10:13], v[54:57], v[26:29], v[10:13]
	ds_read_b128 v[26:29], v65 offset:1024
	v_mfma_f32_16x16x32_f16 v[14:17], v[38:41], v[30:33], v[14:17]
	ds_read_b128 v[38:41], v65 offset:3072
	v_mfma_f32_16x16x32_f16 v[18:21], v[42:45], v[30:33], v[18:21]
	ds_read_b128 v[42:45], v64 offset:17408
	v_mfma_f32_16x16x32_f16 v[22:25], v[50:53], v[30:33], v[22:25]
	ds_read_b128 v[50:53], v64 offset:21504
	ds_read_b128 v[64:67], v64 offset:23552
	v_mfma_f32_16x16x32_f16 v[2:5], v[54:57], v[30:33], v[2:5]
	v_lshlrev_b32_e32 v54, 8, v62
	v_mov_b32_e32 v55, 0
	v_lshl_add_u64 v[56:57], s[0:1], 0, v[54:55]
	s_waitcnt lgkmcnt(0)
	v_mfma_f32_16x16x32_f16 v[6:9], v[42:45], v[26:29], v[6:9]
	v_lshlrev_b32_e32 v54, 2, v1
	v_ashrrev_i32_e32 v1, 31, v0
	v_mfma_f32_16x16x32_f16 v[10:13], v[64:67], v[26:29], v[10:13]
	v_mfma_f32_16x16x32_f16 v[30:33], v[58:61], v[26:29], v[34:37]
	v_mfma_f32_16x16x32_f16 v[34:37], v[50:53], v[26:29], v[46:49]
	s_nop 2
	v_lshlrev_b64 v[48:49], 12, v[0:1]
	v_or_b32_e32 v0, 16, v0
	v_lshl_add_u64 v[46:47], v[56:57], 0, v[54:55]
	v_ashrrev_i32_e32 v1, 31, v0
	v_lshl_add_u64 v[26:27], v[46:47], 0, v[48:49]
	v_lshlrev_b64 v[0:1], 12, v[0:1]
	global_store_dwordx4 v[26:27], v[6:9], off sc1
	global_store_dwordx4 v[26:27], v[10:13], off offset:192 sc1
	global_store_dwordx4 v[26:27], v[30:33], off offset:64 sc1
	v_mfma_f32_16x16x32_f16 v[6:9], v[42:45], v[38:41], v[14:17]
	global_store_dwordx4 v[26:27], v[34:37], off offset:128 sc1
	v_mfma_f32_16x16x32_f16 v[10:13], v[58:61], v[38:41], v[18:21]
	s_nop 2
	v_lshl_add_u64 v[18:19], v[46:47], 0, v[0:1]
	v_mfma_f32_16x16x32_f16 v[14:17], v[50:53], v[38:41], v[22:25]
	s_nop 0
	global_store_dwordx4 v[18:19], v[6:9], off sc1
	s_nop 0
	global_store_dwordx4 v[18:19], v[10:13], off offset:64 sc1
	v_mfma_f32_16x16x32_f16 v[0:3], v[64:67], v[38:41], v[2:5]
	s_nop 2
	global_store_dwordx4 v[18:19], v[14:17], off offset:128 sc1
	s_nop 3
	global_store_dwordx4 v[18:19], v[0:3], off offset:192 sc1
	s_endpgm
